# last 1536 conversion items (layer-1 down weights) moved from the top-k phase into the idle tail of the QKV phase
# baseline (speedup 1.0000x reference)
; #define LAS __attribute__((address_space(3)))
; DI void cvt_resolve(const CvtPtrs& P, int it, const float*& src, int& ldw, bf16_t*& dst, int& ldd, bool& qperm, bool& f8) {
;     int r = it; qperm = false; f8 = false;
;     if (r < 3072) { const int kt = ((r >> 3) / 96) * 8 + (r & 7), nt = (r >> 3) % 96, n0 = nt * 64, part = n0 >> 11, j0 = n0 & 2047;
;         src = P.cin + (size_t)(kt * 64) * 6144 + n0; ldw = 6144; ldd = DM;
;         dst = (part == 0 ? P.W1B + (size_t)j0 * DM : P.W1A + (size_t)((j0 >> 7) * 256 + (part == 2 ? 128 : 0) + (j0 & 127)) * DM) + kt * 64; return; } r -= 3072;
;     if (r < 1024) { const int kt = ((r >> 3) / 32) * 8 + (r & 7), nt = (r >> 3) % 32; src = P.cout + (size_t)(kt * 64) * DM + nt * 64; ldw = DM; dst = P.W2 + (size_t)(nt * 64) * DM + kt * 64; ldd = DM; return; } r -= 1024;
;     if (r < 1536) { const int kt = ((r >> 3) / 48) * 8 + (r & 7), nt = (r >> 3) % 48; src = P.wqkv + (size_t)(kt * 64) * 3072 + nt * 64; ldw = 3072; qperm = nt < 40;     f8 = true; dst = (bf16_t*)((unsigned char*)P.WQKV + (size_t)(nt * 64) * DM + kt * 64); ldd = DM;     return; } r -= 1536;
;     if (r < 1024) { const int kt = ((r >> 3) / 32) * 8 + (r & 7), nt = (r >> 3) % 32; src = P.wo + (size_t)(kt * 64) * DM + nt * 64; ldw = DM; f8 = true;
;         dst = (bf16_t*)((unsigned char*)P.WO + (size_t)(nt * 64) * DM + kt * 64); ldd = DM; return; } r -= 1024;
;     const int l = r / CVT_L, rr = r % CVT_L, kind = rr / 8192, q = rr % 8192, le = l * 16 + q / 512, rem = q % 512;
;     f8 = true;
;     if (kind < 2) { const int kt = ((rem >> 3) / 16) * 8 + (rem & 7), nt = (rem >> 3) % 16, n0 = nt * 64;
;         src = (kind ? P.wu : P.wg) + (size_t)le * DM * DFF + (size_t)(kt * 64) * DFF + n0; ldw = DFF;
;         dst = (bf16_t*)((unsigned char*)P.WGU + (size_t)(le * 2048 + (n0 >> 7) * 256 + kind * 128 + (n0 & 127)) * DM + kt * 64); ldd = DM; }
;     else { const int kt = ((rem >> 3) / 32) * 8 + (rem & 7), nt = (rem >> 3) % 32;
;         src = P.wd + (size_t)le * DFF * DM + (size_t)(kt * 64) * DM + nt * 64; ldw = DM; dst = (bf16_t*)((unsigned char*)P.WDN + (size_t)(le * 2048 + nt * 64) * DFF + kt * 64); ldd = DFF; }
; }
; DI void cvt_range(const CvtPtrs& P, int lo, int hi, int w, int NW, LAS unsigned* scr, int lane) {
;     int it = lo + w; if (it >= hi) return;
;     const int c = lane & 15, q = lane >> 4;
.LBB0_1164:
	s_abs_i32 s0, s33
	v_cvt_f32_u32_e32 v2, s0
	s_add_i32 s1, s33, 0x31f
	s_xor_b32 s10, s1, s33
	s_sub_i32 s11, 0, s0
	v_rcp_iflag_f32_e32 v2, v2
	s_ashr_i32 s16, s10, 31
	s_abs_i32 s1, s1
	v_mul_f32_e32 v2, 0x4f7ffffe, v2
	v_cvt_u32_f32_e32 v2, v2
	s_nop 0
	v_readfirstlane_b32 s10, v2
	s_mul_i32 s11, s11, s10
	s_mul_hi_u32 s11, s10, s11
	s_add_i32 s10, s10, s11
	s_mul_hi_u32 s10, s1, s10
	s_mul_i32 s11, s10, s0
	s_sub_i32 s1, s1, s11
	s_add_i32 s12, s10, 1
	s_sub_i32 s11, s1, s0
	s_cmp_ge_u32 s1, s0
	s_cselect_b32 s10, s12, s10
	s_cselect_b32 s1, s11, s1
	s_add_i32 s11, s10, 1
	s_cmp_ge_u32 s1, s0
	s_cselect_b32 s0, s11, s10
	s_xor_b32 s17, s0, s16
	s_sub_i32 s18, s17, s16
	s_add_i32 s19, s18, -1
	s_mul_i32 s19, s19, s33
	s_sub_i32 s20, 0x320, s19
	s_cmp_lt_i32 s2, s20
	s_cbranch_scc1 .LBB0_1209
	s_sub_i32 s0, s2, s20
	s_lshl_b32 s0, s0, 3
	v_readlane_b32 s1, v251, 25
	s_add_i32 s0, s0, s1
	s_cmpk_gt_u32 s0, 0x233f
	s_cbranch_scc1 .LBB0_1209
	s_add_i32 s12, s0, 0x3cc0
	s_bfe_u32 s1, s12, 0x40009
	s_bfe_u32 s28, s88, 0x30006
	s_or_b32 s13, s1, 16
	s_mov_b32 s30, s88
	s_cmpk_gt_u32 s0, 0x33f
	s_cbranch_scc0 .LBB0_1168
	v_readlane_b32 s44, v251, 28
	s_lshr_b32 s0, s12, 5
	v_readlane_b32 s48, v251, 32
	v_readlane_b32 s49, v251, 33
	s_and_b32 s0, s0, 8
	v_readlane_b32 s50, v251, 34
	v_readlane_b32 s51, v251, 35
	s_mov_b64 s[24:25], s[48:49]
	s_or_b32 s0, s0, s28
	s_lshl_b32 s1, s13, 23
	s_mov_b64 s[26:27], s[50:51]
	s_add_u32 s1, s26, s1
	s_addc_u32 s14, s27, 0
	s_lshl_b32 s10, s0, 6
	s_lshl_b32 s0, s0, 19
	s_add_u32 s0, s1, s0
	s_addc_u32 s1, s14, 0
	s_lshl_b32 s14, s12, 3
	s_and_b32 s21, s14, 0x7c0
	s_lshl_b32 s14, s21, 2
	s_add_u32 s14, s0, s14
	s_addc_u32 s15, s1, 0
	s_lshl_b32 s0, s13, 21
	s_lshl_b32 s1, s21, 10
	s_mov_b32 s11, 0
	v_readlane_b32 s45, v251, 29
	v_readlane_b32 s46, v251, 30
	v_readlane_b32 s47, v251, 31
	s_or_b32 s21, s0, s1
	s_mov_b64 s[0:1], 0
	s_branch .LBB0_1169

; #define LAS __attribute__((address_space(3)))
; #define LDS_WAIT() asm volatile("s_waitcnt lgkmcnt(0)" ::: "memory")
; DI void cvt_range(const CvtPtrs& P, int lo, int hi, int w, int NW, LAS unsigned* scr, int lane) {
;     ...
;         const int nit = it + NW; bf16_t* cdst = dst; const int cldd = ldd;
;         if (nit < hi) { cvt_resolve(P, nit, src, ldw, dst, ldd, qperm, f8);
; #pragma unroll
;             for (int rr = 0; rr < 16; ++rr) v[rr] = __builtin_nontemporal_load((const f32x4*)(src + (size_t)(16 * q + rr) * ldw + 4 * c)); }
;         if (cf8) {
; #pragma unroll
;             for (int i = 0; i < 4; ++i) *(LAS u32x4*)(scr + (wrow + i) * 20 + 4 * q) = pa[i];
;             LDS_WAIT(); asm volatile("" ::: "memory");
; #pragma unroll
;             for (int j = 0; j < 4; ++j) { const int ch = lane + 64 * j, n = ch >> 2, part = ch & 3; const u32x4 o = *(const LAS u32x4*)(scr + n * 20 + 4 * part);
;                 *(u32x4*)((unsigned char*)cdst + (size_t)n * cldd + 16 * part) = o; }
;         } else {
; #pragma unroll
;             for (int i = 0; i < 4; ++i) { *(LAS u32x4*)(scr + (wrow + i) * CVT_P + 8 * q) = pa[i]; *(LAS u32x4*)(scr + (wrow + i) * CVT_P + 8 * q + 4) = pb[i]; }
;             LDS_WAIT(); asm volatile("" ::: "memory");
; #pragma unroll
;             for (int j = 0; j < 8; ++j) { const int n = (lane >> 3) + 8 * j; const u32x4 o = *(const LAS u32x4*)(scr + n * CVT_P + 4 * (lane & 7));
;                 *(u32x4*)(cdst + (size_t)n * cldd + 8 * (lane & 7)) = o; }
;         }
;         LDS_WAIT(); asm volatile("" ::: "memory");
;         if (nit >= hi) break;
;         it = nit;
.LBB0_1173:
	s_waitcnt lgkmcnt(0)
	s_add_i32 s3, s3, s30
	s_add_i32 s34, s34, s35
	s_add_i32 s36, s36, s30
	s_add_i32 s37, s37, s38
	s_add_i32 s10, s85, s3
	s_cmp_lt_i32 s10, 0xda00
	s_mov_b64 s[10:11], s[18:19]
	s_mov_b32 s29, s0
	s_mov_b64 s[12:13], s[20:21]
	s_mov_b64 s[14:15], s[16:17]
	s_cbranch_scc0 .LBB0_1208

; DI void cvt_resolve(const CvtPtrs& P, int it, const float*& src, int& ldw, bf16_t*& dst, int& ldd, bool& qperm, bool& f8) {
;     int r = it; qperm = false; f8 = false;
;     if (r < 3072) { const int kt = ((r >> 3) / 96) * 8 + (r & 7), nt = (r >> 3) % 96, n0 = nt * 64, part = n0 >> 11, j0 = n0 & 2047;
;         src = P.cin + (size_t)(kt * 64) * 6144 + n0; ldw = 6144; ldd = DM;
;         dst = (part == 0 ? P.W1B + (size_t)j0 * DM : P.W1A + (size_t)((j0 >> 7) * 256 + (part == 2 ? 128 : 0) + (j0 & 127)) * DM) + kt * 64; return; } r -= 3072;
;     if (r < 1024) { const int kt = ((r >> 3) / 32) * 8 + (r & 7), nt = (r >> 3) % 32; src = P.cout + (size_t)(kt * 64) * DM + nt * 64; ldw = DM; dst = P.W2 + (size_t)(nt * 64) * DM + kt * 64; ldd = DM; return; } r -= 1024;
;     if (r < 1536) { const int kt = ((r >> 3) / 48) * 8 + (r & 7), nt = (r >> 3) % 48; src = P.wqkv + (size_t)(kt * 64) * 3072 + nt * 64; ldw = 3072; qperm = nt < 40;     f8 = true; dst = (bf16_t*)((unsigned char*)P.WQKV + (size_t)(nt * 64) * DM + kt * 64); ldd = DM;     return; } r -= 1536;
;     if (r < 1024) { const int kt = ((r >> 3) / 32) * 8 + (r & 7), nt = (r >> 3) % 32; src = P.wo + (size_t)(kt * 64) * DM + nt * 64; ldw = DM; f8 = true;
;         dst = (bf16_t*)((unsigned char*)P.WO + (size_t)(nt * 64) * DM + kt * 64); ldd = DM; return; } r -= 1024;
;     const int l = r / CVT_L, rr = r % CVT_L, kind = rr / 8192, q = rr % 8192, le = l * 16 + q / 512, rem = q % 512;
;     f8 = true;
;     if (kind < 2) { const int kt = ((rem >> 3) / 16) * 8 + (rem & 7), nt = (rem >> 3) % 16, n0 = nt * 64;
;         src = (kind ? P.wu : P.wg) + (size_t)le * DM * DFF + (size_t)(kt * 64) * DFF + n0; ldw = DFF;
;         dst = (bf16_t*)((unsigned char*)P.WGU + (size_t)(le * 2048 + (n0 >> 7) * 256 + kind * 128 + (n0 & 127)) * DM + kt * 64); ldd = DM; }
;     else { const int kt = ((rem >> 3) / 32) * 8 + (rem & 7), nt = (rem >> 3) % 32;
;         src = P.wd + (size_t)le * DFF * DM + (size_t)(kt * 64) * DM + nt * 64; ldw = DM; dst = (bf16_t*)((unsigned char*)P.WDN + (size_t)(le * 2048 + nt * 64) * DFF + kt * 64); ldd = DFF; }
; }
.LBB0_1178:
	s_add_i32 s69, s85, s36
	s_add_i32 s68, s69, 0x84c0
	s_cmp_gt_i32 s68, 0xd9ff
	s_mov_b64 s[16:17], s[14:15]
	s_mov_b64 s[20:21], s[12:13]
	s_mov_b32 s0, s29
	s_mov_b64 s[18:19], s[10:11]
	s_cbranch_scc1 .LBB0_1204
	s_cmpk_gt_i32 s68, 0xbff
	s_mov_b64 s[26:27], -1
	s_cbranch_scc0 .LBB0_1197
	s_mov_b64 s[16:17], -1
	s_cmpk_gt_u32 s68, 0xfff
	s_cbranch_scc0 .LBB0_1194
	s_cmpk_gt_u32 s68, 0x15ff
	s_mov_b64 s[20:21], -1
	s_cbranch_scc0 .LBB0_1192
	s_cmpk_gt_u32 s68, 0x19ff
	s_cbranch_scc0 .LBB0_1189
	s_add_i32 s18, s69, 0x6ac0
	s_add_i32 s0, s69, 0xac0
	s_cmpk_lt_u32 s18, 0x6000
	s_cselect_b32 s0, s18, s0
	s_cmpk_gt_u32 s18, 0x5fff
	s_cselect_b32 s18, 16, 0
	s_bfe_u32 s19, s0, 0x40009
	s_or_b32 s21, s19, s18
	s_and_b32 s22, s0, 7
	s_cmpk_gt_u32 s0, 0x3fff
	s_mov_b64 s[18:19], -1
	s_cbranch_scc0 .LBB0_1185
	s_lshr_b32 s18, s0, 5
	s_and_b32 s18, s18, 8
	v_readlane_b32 s52, v251, 28
	s_or_b32 s18, s18, s22
	s_lshl_b32 s19, s21, 23
	v_readlane_b32 s58, v251, 34
	v_readlane_b32 s59, v251, 35
	s_add_u32 s19, s58, s19
	s_addc_u32 s23, s59, 0
	s_lshl_b32 s20, s18, 6
	s_lshl_b32 s18, s18, 19
	s_add_u32 s18, s19, s18
	s_addc_u32 s19, s23, 0
	s_lshl_b32 s23, s0, 3
	s_and_b32 s23, s23, 0x7c0
	s_lshl_b32 s24, s23, 2
	s_add_u32 s24, s18, s24
	s_addc_u32 s25, s19, 0
	s_lshl_b32 s18, s21, 21
	s_lshl_b32 s19, s23, 10
	v_readlane_b32 s53, v251, 29
	v_readlane_b32 s54, v251, 30
	v_readlane_b32 s55, v251, 31
	v_readlane_b32 s56, v251, 32
	v_readlane_b32 s57, v251, 33
	s_or_b32 s26, s18, s19
	s_mov_b64 s[18:19], 0

; #define LAS __attribute__((address_space(3)))
; DI void cvt_resolve(const CvtPtrs& P, int it, const float*& src, int& ldw, bf16_t*& dst, int& ldd, bool& qperm, bool& f8) {
;     int r = it; qperm = false; f8 = false;
;     if (r < 3072) { const int kt = ((r >> 3) / 96) * 8 + (r & 7), nt = (r >> 3) % 96, n0 = nt * 64, part = n0 >> 11, j0 = n0 & 2047;
;         src = P.cin + (size_t)(kt * 64) * 6144 + n0; ldw = 6144; ldd = DM;
;         dst = (part == 0 ? P.W1B + (size_t)j0 * DM : P.W1A + (size_t)((j0 >> 7) * 256 + (part == 2 ? 128 : 0) + (j0 & 127)) * DM) + kt * 64; return; } r -= 3072;
;     if (r < 1024) { const int kt = ((r >> 3) / 32) * 8 + (r & 7), nt = (r >> 3) % 32; src = P.cout + (size_t)(kt * 64) * DM + nt * 64; ldw = DM; dst = P.W2 + (size_t)(nt * 64) * DM + kt * 64; ldd = DM; return; } r -= 1024;
;     if (r < 1536) { const int kt = ((r >> 3) / 48) * 8 + (r & 7), nt = (r >> 3) % 48; src = P.wqkv + (size_t)(kt * 64) * 3072 + nt * 64; ldw = 3072; qperm = nt < 40;     f8 = true; dst = (bf16_t*)((unsigned char*)P.WQKV + (size_t)(nt * 64) * DM + kt * 64); ldd = DM;     return; } r -= 1536;
;     if (r < 1024) { const int kt = ((r >> 3) / 32) * 8 + (r & 7), nt = (r >> 3) % 32; src = P.wo + (size_t)(kt * 64) * DM + nt * 64; ldw = DM; f8 = true;
;         dst = (bf16_t*)((unsigned char*)P.WO + (size_t)(nt * 64) * DM + kt * 64); ldd = DM; return; } r -= 1024;
;     const int l = r / CVT_L, rr = r % CVT_L, kind = rr / 8192, q = rr % 8192, le = l * 16 + q / 512, rem = q % 512;
;     f8 = true;
;     if (kind < 2) { const int kt = ((rem >> 3) / 16) * 8 + (rem & 7), nt = (rem >> 3) % 16, n0 = nt * 64;
;         src = (kind ? P.wu : P.wg) + (size_t)le * DM * DFF + (size_t)(kt * 64) * DFF + n0; ldw = DFF;
;         dst = (bf16_t*)((unsigned char*)P.WGU + (size_t)(le * 2048 + (n0 >> 7) * 256 + kind * 128 + (n0 & 127)) * DM + kt * 64); ldd = DM; }
;     else { const int kt = ((rem >> 3) / 32) * 8 + (rem & 7), nt = (rem >> 3) % 32;
; __global__ void __launch_bounds__(512, 2) dit_fwd(Args args) {
;     ...
;     PHASE(15) { REP_BAR(); ph_topk(128, affL, affC, rowsrc, gatev, inv, (LAS unsigned*)lds, tid, lane, wave, bid, G); CVT(C11, GU1_END);
;         if (C11 >= GU1_END) { if (G <= 128) CVT(C11, CVT_TOTAL); else if (bid >= 128) { CVT_MKCP(); cvt_range(CP, C11, CVT_TOTAL, (bid - 128) * 8 + wave, (G - 128) * 8, cscr, lane); } }
.LBB0_1718:
	s_cmpk_gt_i32 s33, 0x80
	s_mov_b64 s[36:37], -1
	s_cbranch_scc0 .LBB0_1767
	s_add_i32 s14, s86, 0xfffffc00
	s_cmp_eq_u32 s14, s14
	s_cselect_b64 s[36:37], -1, 0
	s_or_b64 s[36:37], s[50:51], s[36:37]
	s_and_b64 vcc, exec, s[36:37]
	s_cbranch_vccnz .LBB0_1766
	v_readlane_b32 s56, v251, 40
	s_add_i32 s76, s56, 0xd000
	s_cmp_gt_i32 s14, 0xffff37ff
	v_readlane_b32 s57, v251, 41
	s_cbranch_scc0 .LBB0_1725
	s_add_i32 s15, s56, 0xc400
	s_lshr_b32 s15, s15, 5
	s_and_b32 s15, s15, 0x3fffff8
	v_readlane_b32 s16, v251, 42
	s_or_b32 s15, s84, s15
	v_readlane_b32 s22, v251, 48
	v_readlane_b32 s23, v251, 49
	s_lshl_b32 s14, s76, 3
	s_mov_b32 s37, 0
	s_lshl_b32 s36, s15, 6
	v_readlane_b32 s20, v251, 46
	v_readlane_b32 s21, v251, 47
	s_mov_b64 s[70:71], s[22:23]
	s_and_b32 s14, s14, 0x7c0
	s_lshl_b64 s[38:39], s[36:37], 13
	s_mov_b64 s[68:69], s[20:21]
	s_add_u32 s38, s68, s38
	s_addc_u32 s39, s69, s39
	s_lshl_b32 s15, s14, 2
	s_add_u32 s58, s38, s15
	s_addc_u32 s59, s39, 0
	s_lshl_b32 s38, s14, 12
	s_add_u32 s38, s3, s38
	s_addc_u32 s39, s90, 0
	s_lshl_b64 s[36:37], s[36:37], 1
	s_add_u32 s36, s38, s36
	s_addc_u32 s37, s39, s37
	v_readlane_b32 s30, v251, 56
	v_readlane_b32 s31, v251, 57
	s_cmpk_lt_u32 s76, 0x1000
	s_mov_b64 s[52:53], 0
	v_readlane_b32 s17, v251, 43
	v_readlane_b32 s18, v251, 44
	v_readlane_b32 s19, v251, 45
	v_readlane_b32 s24, v251, 50
	v_readlane_b32 s25, v251, 51
	v_readlane_b32 s26, v251, 52
	v_readlane_b32 s27, v251, 53
	v_readlane_b32 s28, v251, 54
	v_readlane_b32 s29, v251, 55
	s_cbranch_scc1 .LBB0_1726
	s_bfe_u32 s38, s56, 0x80003
	s_add_i32 s37, s76, 0xf000
	s_mulk_i32 s38, 0xab
	s_and_b32 s37, s37, 0xffff
	s_lshr_b32 s38, s38, 13
	s_lshr_b32 s36, s56, 3
	s_mul_i32 s37, s37, 0xaaab
	s_mul_i32 s38, s38, 48
	s_sub_i32 s36, s36, s38
	s_lshr_b32 s37, s37, 24
	s_lshl_b32 s38, s76, 6
	s_lshl_b32 s37, s37, 9
	s_and_b32 s38, s38, 0x1c0
	s_or_b32 s37, s37, s38
	s_mul_i32 s38, s37, 0x3000
	s_add_u32 s38, s70, s38
	s_addc_u32 s39, s71, 0
	s_and_b32 s36, s36, 0xff
	s_lshl_b32 s50, s36, 8
	s_add_u32 s58, s38, s50
	s_addc_u32 s59, s39, 0
	s_cmp_lt_u32 s36, 40
	s_cselect_b64 s[38:39], -1, 0
	s_lshl_b32 s36, s36, 17
	v_readlane_b32 s16, v250, 9
	s_add_u32 s36, s16, s36
	v_readlane_b32 s16, v250, 4
	s_addc_u32 s50, s16, 0
	s_add_u32 s36, s36, s37
	s_addc_u32 s37, s50, 0
	s_cmpk_lt_u32 s76, 0x1600
	s_cbranch_scc1 .LBB0_1776
	s_lshr_b32 s36, s96, 5
	s_and_b32 s36, s36, 0x3fffff8
	s_or_b32 s36, s84, s36
	s_lshl_b32 s36, s36, 6
	s_mov_b32 s37, 0
	s_mov_b64 s[78:79], s[30:31]
	s_lshl_b64 s[38:39], s[36:37], 13
	s_add_u32 s37, s78, s38
	s_addc_u32 s38, s79, s39
	s_add_u32 s58, s37, s15
	s_addc_u32 s59, s38, 0
	s_lshl_b32 s14, s14, 11
	v_readlane_b32 s15, v250, 5
	s_add_u32 s14, s15, s14
	v_readlane_b32 s15, v250, 6
	s_addc_u32 s15, s15, 0
	s_add_u32 s36, s14, s36
	s_addc_u32 s37, s15, 0
	s_cmpk_lt_u32 s76, 0x1a00
	s_cbranch_scc1 .LBB0_1778
	s_add_i32 s14, s56, 0xb600
	s_add_i32 s15, s56, 0x5600
	s_cmpk_lt_u32 s14, 0x6000
	s_cselect_b32 s36, s14, s15
	s_cmpk_gt_u32 s14, 0x5fff
	s_cselect_b32 s14, 16, 0
	s_bfe_u32 s15, s36, 0x40009
	s_or_b32 s37, s15, s14
	s_cmpk_lt_u32 s36, 0x4000
	s_cselect_b64 s[14:15], -1, 0
	s_lshr_b32 s39, s36, 5
	s_and_b32 s38, s36, 7
	s_and_b32 s39, s39, 8
	v_readlane_b32 s20, v251, 28
	s_or_b32 s39, s39, s38
	s_lshl_b32 s50, s37, 23
	v_readlane_b32 s26, v251, 34
	v_readlane_b32 s27, v251, 35
	s_add_u32 s51, s26, s50
	s_addc_u32 s56, s27, 0
	s_lshl_b32 s57, s39, 6
	s_lshl_b32 s39, s39, 19
	s_add_u32 s39, s51, s39
	s_addc_u32 s51, s56, 0
	s_lshl_b32 s56, s36, 3
	s_and_b32 s58, s56, 0x7c0
	s_lshl_b32 s59, s58, 2
	s_add_u32 s39, s39, s59
	s_addc_u32 s51, s51, 0
	s_lshl_b32 s59, s37, 21
	s_lshl_b32 s58, s58, 10
	s_or_b32 s58, s59, s58
	s_lshr_b32 s59, s36, 4
	s_and_b32 s59, s59, 24
	s_or_b32 s38, s59, s38
	v_readlane_b32 s22, v251, 30
	v_readlane_b32 s24, v251, 32
	s_cmpk_lt_u32 s36, 0x2000
	v_readlane_b32 s23, v251, 31
	v_readlane_b32 s25, v251, 33
	s_cselect_b32 s64, s22, s24
	s_cselect_b32 s59, s23, s25
	s_add_u32 s50, s64, s50
	s_addc_u32 s59, s59, 0
	s_lshl_b32 s64, s38, 6
	s_lshl_b32 s38, s38, 18
	s_add_u32 s38, s50, s38
	s_addc_u32 s50, s59, 0
	s_lshl_b32 s59, s36, 5
	s_and_b32 s59, s59, 0xf00
	s_add_u32 s38, s38, s59
	s_addc_u32 s50, s50, 0
	s_lshl_b32 s59, s36, 4
	s_lshl_b32 s37, s37, 11
	s_and_b32 s59, s59, 0x700
	s_lshr_b32 s36, s36, 6
	s_or_b32 s37, s37, s59
	s_and_b32 s36, s36, 0x80
	s_or_b32 s36, s37, s36
	s_and_b32 s37, s56, 64
	s_or_b32 s36, s36, s37
	s_lshl_b32 s36, s36, 11
	s_and_b64 s[14:15], s[14:15], exec
	v_readlane_b32 s15, v250, 8
	v_readlane_b32 s16, v250, 11
	s_cselect_b32 s15, s15, s16
	v_readlane_b32 s16, v250, 7
	v_readlane_b32 s17, v250, 10
	s_cselect_b32 s14, s36, s58
	s_cselect_b32 s36, s16, s17
	s_cselect_b32 s58, s38, s39
	s_movk_i32 s38, 0x400
	s_cselect_b32 s37, 0, 0
	s_cselect_b32 s57, s64, s57
	s_cselect_b32 s59, s50, s51
	s_cselect_b32 s56, s38, 0x800
	s_cselect_b32 s77, 0x800, s38
	s_add_u32 s14, s36, s14
	s_addc_u32 s15, s15, 0
	s_add_u32 s36, s14, s57
	s_addc_u32 s37, s15, s37
	v_readlane_b32 s21, v251, 29
	s_branch .LBB0_1779
